# indexer step 1: first-4 scores converted with v_cvt_pk_f16_f32 directly on the non-diagonal path (scalar converts moved to the diagonal path); per-tile s[0:1] flag moves dropped
# baseline (speedup 1.0000x reference)
.LBB0_382:
	s_cmp_eq_u32 s81, s0
	v_mfma_f32_32x32x16_bf16 v[10:25], v[80:83], v[84:87], 0
	v_mfma_f32_32x32x16_bf16 v[10:25], v[76:79], v[88:91], v[10:25]
	v_mfma_f32_32x32x16_bf16 v[10:25], v[72:75], v[92:95], v[10:25]
	v_mfma_f32_32x32x16_bf16 v[10:25], v[52:55], v[96:99], v[10:25]
	s_nop 11
	v_fma_f32 v48, |v10|, v2, 0
	v_fma_f32 v49, |v11|, v2, 0
	v_fma_f32 v50, |v12|, v2, 0
	v_fma_f32 v51, |v13|, v2, 0
	v_fma_f32 v212, |v14|, v2, 0
	v_fma_f32 v213, |v15|, v2, 0
	v_fma_f32 v215, |v16|, v2, 0
	v_fma_f32 v216, |v17|, v2, 0
	v_fma_f32 v217, |v18|, v2, 0
	v_fma_f32 v228, |v19|, v2, 0
	v_mfma_f32_32x32x16_bf16 v[4:19], v[80:83], v[100:103], 0
	v_fma_f32 v229, |v20|, v2, 0
	v_fma_f32 v230, |v21|, v2, 0
	v_mfma_f32_32x32x16_bf16 v[4:19], v[76:79], v[104:107], v[4:19]
	v_fma_f32 v234, |v22|, v2, 0
	v_fma_f32 v235, |v23|, v2, 0
	v_mfma_f32_32x32x16_bf16 v[4:19], v[72:75], v[108:111], v[4:19]
	v_fma_f32 v236, |v24|, v2, 0
	v_fma_f32 v237, |v25|, v2, 0
	v_mfma_f32_32x32x16_bf16 v[4:19], v[52:55], v[112:115], v[4:19]
	s_nop 11
	v_fma_f32 v48, |v4|, v249, v48
	v_mfma_f32_32x32x16_bf16 v[20:35], v[80:83], v[116:119], 0
	v_fma_f32 v49, |v5|, v249, v49
	v_fma_f32 v50, |v6|, v249, v50
	v_fma_f32 v51, |v7|, v249, v51
	v_mfma_f32_32x32x16_bf16 v[20:35], v[76:79], v[120:123], v[20:35]
	v_fma_f32 v8, |v8|, v249, v212
	v_fma_f32 v9, |v9|, v249, v213
	v_fma_f32 v10, |v10|, v249, v215
	v_fma_f32 v11, |v11|, v249, v216
	v_mfma_f32_32x32x16_bf16 v[20:35], v[72:75], v[124:127], v[20:35]
	v_fma_f32 v12, |v12|, v249, v217
	v_fma_f32 v13, |v13|, v249, v228
	v_fma_f32 v212, |v14|, v249, v229
	v_fma_f32 v213, |v15|, v249, v230
	v_fma_f32 v215, |v16|, v249, v234
	v_fma_f32 v216, |v17|, v249, v235
	v_fma_f32 v217, |v18|, v249, v236
	v_fma_f32 v228, |v19|, v249, v237
	v_mfma_f32_32x32x16_bf16 v[20:35], v[52:55], v[128:131], v[20:35]
	s_nop 11
	v_fma_f32 v24, |v24|, v250, v8
	v_fma_f32 v25, |v25|, v250, v9
	v_fma_f32 v26, |v26|, v250, v10
	v_fma_f32 v27, |v27|, v250, v11
	v_fma_f32 v28, |v28|, v250, v12
	v_fma_f32 v29, |v29|, v250, v13
	v_mfma_f32_32x32x16_bf16 v[4:19], v[80:83], v[132:135], 0
	v_fma_f32 v48, |v20|, v250, v48
	v_fma_f32 v49, |v21|, v250, v49
	v_fma_f32 v50, |v22|, v250, v50
	v_fma_f32 v51, |v23|, v250, v51
	v_mfma_f32_32x32x16_bf16 v[4:19], v[76:79], v[136:139], v[4:19]
	v_fma_f32 v212, |v30|, v250, v212
	v_mfma_f32_32x32x16_bf16 v[4:19], v[72:75], v[140:143], v[4:19]
	v_fma_f32 v213, |v31|, v250, v213
	v_fma_f32 v215, |v32|, v250, v215
	v_fma_f32 v216, |v33|, v250, v216
	v_fma_f32 v217, |v34|, v250, v217
	v_fma_f32 v228, |v35|, v250, v228
	v_mfma_f32_32x32x16_bf16 v[4:19], v[52:55], v[144:147], v[4:19]
	s_nop 11
	v_fma_f32 v229, |v8|, v251, v24
	v_fma_f32 v230, |v9|, v251, v25
	v_fma_f32 v234, |v10|, v251, v26
	v_fma_f32 v235, |v11|, v251, v27
	v_fma_f32 v236, |v12|, v251, v28
	v_fma_f32 v237, |v13|, v251, v29
	v_mfma_f32_32x32x16_bf16 v[20:35], v[80:83], v[148:151], 0
	v_fma_f32 v48, |v4|, v251, v48
	v_fma_f32 v49, |v5|, v251, v49
	v_fma_f32 v50, |v6|, v251, v50
	v_fma_f32 v51, |v7|, v251, v51
	v_mfma_f32_32x32x16_bf16 v[20:35], v[76:79], v[152:155], v[20:35]
	v_fma_f32 v212, |v14|, v251, v212
	v_mfma_f32_32x32x16_bf16 v[20:35], v[72:75], v[156:159], v[20:35]
	v_fma_f32 v213, |v15|, v251, v213
	v_fma_f32 v215, |v16|, v251, v215
	v_fma_f32 v216, |v17|, v251, v216
	v_fma_f32 v217, |v18|, v251, v217
	v_fma_f32 v228, |v19|, v251, v228
	v_mfma_f32_32x32x16_bf16 v[20:35], v[52:55], v[160:163], v[20:35]
	s_nop 11
	v_fma_f32 v20, |v20|, v252, v48
	v_fma_f32 v21, |v21|, v252, v49
	v_fma_f32 v22, |v22|, v252, v50
	v_fma_f32 v23, |v23|, v252, v51
	v_mfma_f32_32x32x16_bf16 v[36:51], v[80:83], v[164:167], 0
	v_fma_f32 v24, |v24|, v252, v229
	v_fma_f32 v25, |v25|, v252, v230
	v_mfma_f32_32x32x16_bf16 v[36:51], v[76:79], v[168:171], v[36:51]
	v_fma_f32 v26, |v26|, v252, v234
	v_fma_f32 v27, |v27|, v252, v235
	v_mfma_f32_32x32x16_bf16 v[36:51], v[72:75], v[172:175], v[36:51]
	v_fma_f32 v229, |v28|, v252, v236
	v_fma_f32 v230, |v29|, v252, v237
	v_fma_f32 v212, |v30|, v252, v212
	v_fma_f32 v213, |v31|, v252, v213
	v_fma_f32 v215, |v32|, v252, v215
	v_fma_f32 v216, |v33|, v252, v216
	v_fma_f32 v217, |v34|, v252, v217
	v_fma_f32 v228, |v35|, v252, v228
	v_mfma_f32_32x32x16_bf16 v[36:51], v[52:55], v[176:179], v[36:51]
	s_nop 11
	v_fma_f32 v234, |v36|, v253, v20
	v_fma_f32 v235, |v37|, v253, v21
	v_fma_f32 v236, |v38|, v253, v22
	v_fma_f32 v237, |v39|, v253, v23
	v_fma_f32 v40, |v40|, v253, v24
	v_fma_f32 v41, |v41|, v253, v25
	v_fma_f32 v42, |v42|, v253, v26
	v_fma_f32 v43, |v43|, v253, v27
	v_mfma_f32_32x32x16_bf16 v[12:27], v[80:83], v[180:183], 0
	v_fma_f32 v44, |v44|, v253, v229
	v_fma_f32 v45, |v45|, v253, v230
	v_mfma_f32_32x32x16_bf16 v[12:27], v[76:79], v[184:187], v[12:27]
	v_fma_f32 v46, |v46|, v253, v212
	v_fma_f32 v47, |v47|, v253, v213
	v_mfma_f32_32x32x16_bf16 v[12:27], v[72:75], v[188:191], v[12:27]
	v_fma_f32 v48, |v48|, v253, v215
	v_fma_f32 v49, |v49|, v253, v216
	v_fma_f32 v50, |v50|, v253, v217
	v_fma_f32 v51, |v51|, v253, v228
	v_mfma_f32_32x32x16_bf16 v[12:27], v[52:55], v[192:195], v[12:27]
	s_nop 11
	v_fma_f32 v212, |v12|, v223, v234
	v_fma_f32 v213, |v13|, v223, v235
	v_fma_f32 v215, |v14|, v223, v236
	v_fma_f32 v216, |v15|, v223, v237
	v_fma_f32 v217, |v16|, v223, v40
	v_fma_f32 v228, |v17|, v223, v41
	v_fma_f32 v229, |v18|, v223, v42
	v_fma_f32 v230, |v19|, v223, v43
	v_mfma_f32_32x32x16_bf16 v[4:19], v[80:83], v[196:199], 0
	v_fma_f32 v234, |v20|, v223, v44
	v_fma_f32 v235, |v21|, v223, v45
	v_mfma_f32_32x32x16_bf16 v[4:19], v[76:79], v[200:203], v[4:19]
	v_fma_f32 v236, |v22|, v223, v46
	v_fma_f32 v237, |v23|, v223, v47
	v_mfma_f32_32x32x16_bf16 v[4:19], v[72:75], v[204:207], v[4:19]
	v_fma_f32 v48, |v24|, v223, v48
	v_fma_f32 v49, |v25|, v223, v49
	v_fma_f32 v50, |v26|, v223, v50
	v_fma_f32 v51, |v27|, v223, v51
	v_mfma_f32_32x32x16_bf16 v[4:19], v[52:55], v[208:211], v[4:19]
	ds_read_b128 v[20:23], v214 offset:32768
	ds_read_b128 v[36:39], v214 offset:33792
	ds_read_b128 v[40:43], v214 offset:34816
	ds_read_b128 v[44:47], v214 offset:35840
	s_waitcnt lgkmcnt(3)
	v_mfma_f32_32x32x16_bf16 v[20:35], v[80:83], v[20:23], 0
	s_nop 5
	v_fma_f32 v212, |v4|, v219, v212
	v_fma_f32 v213, |v5|, v219, v213
	v_fma_f32 v4, |v6|, v219, v215
	v_fma_f32 v5, |v7|, v219, v216
	s_waitcnt lgkmcnt(2)
	v_mfma_f32_32x32x16_bf16 v[20:35], v[76:79], v[36:39], v[20:35]
	v_fma_f32 v6, |v8|, v219, v217
	v_fma_f32 v7, |v9|, v219, v228
	v_fma_f32 v8, |v10|, v219, v229
	v_fma_f32 v9, |v11|, v219, v230
	s_waitcnt lgkmcnt(1)
	v_mfma_f32_32x32x16_bf16 v[20:35], v[72:75], v[40:43], v[20:35]
	v_fma_f32 v36, |v12|, v219, v234
	v_fma_f32 v37, |v13|, v219, v235
	v_fma_f32 v38, |v14|, v219, v236
	v_fma_f32 v39, |v15|, v219, v237
	s_waitcnt lgkmcnt(0)
	v_mfma_f32_32x32x16_bf16 v[20:35], v[52:55], v[44:47], v[20:35]
	v_fma_f32 v16, |v16|, v219, v48
	v_fma_f32 v17, |v17|, v219, v49
	s_nop 9
	v_add_f32_e32 v20, v212, v20
	v_pk_add_f32 v[14:15], v[4:5], v[22:23]
	v_pk_add_f32 v[4:5], v[32:33], v[16:17]
	v_fma_f32 v18, |v18|, v219, v50
	v_fma_f32 v19, |v19|, v219, v51
	v_add_f32_e32 v21, v213, v21
	v_add_f32_e32 v17, v34, v18
	v_add_f32_e32 v19, v35, v19
	v_pk_add_f32 v[10:11], v[8:9], v[26:27]
	v_pk_add_f32 v[8:9], v[36:37], v[28:29]
	v_pk_add_f32 v[12:13], v[6:7], v[24:25]
	v_pk_add_f32 v[6:7], v[38:39], v[30:31]
	s_cbranch_scc1 .LBB0_384
	v_cvt_pk_f16_f32 v23, v6, v7
	v_pk_ashrrev_i16 v24, 15, v23 op_sel_hi:[0,1]
	v_bitop3_b32 v7, v23, v24, s32 bitop3:0x1e
	v_bfe_u32 v24, v7, 8, 8
	v_lshrrev_b32_e32 v23, 24, v7
	v_lshl_add_u32 v24, v24, 2, v222
	v_lshl_add_u32 v23, v23, 2, v222
	ds_add_u32 v24, v224 offset:36864
	ds_add_u32 v23, v224 offset:36864
	v_cvt_pk_f16_f32 v25, v8, v9
	v_pk_ashrrev_i16 v27, 15, v25 op_sel_hi:[0,1]
	v_bitop3_b32 v6, v25, v27, s32 bitop3:0x1e
	v_bfe_u32 v27, v6, 8, 8
	v_lshrrev_b32_e32 v25, 24, v6
	v_lshl_add_u32 v27, v27, 2, v222
	v_lshl_add_u32 v25, v25, 2, v222
	ds_add_u32 v27, v224 offset:36864
	ds_add_u32 v25, v224 offset:36864
	v_cvt_pk_f16_f32 v28, v10, v11
	v_pk_ashrrev_i16 v32, 15, v28 op_sel_hi:[0,1]
	v_bitop3_b32 v9, v28, v32, s32 bitop3:0x1e
	v_bfe_u32 v32, v9, 8, 8
	v_lshrrev_b32_e32 v28, 24, v9
	v_lshl_add_u32 v32, v32, 2, v222
	v_lshl_add_u32 v28, v28, 2, v222
	ds_add_u32 v32, v224 offset:36864
	ds_add_u32 v28, v224 offset:36864
	v_cvt_pk_f16_f32 v33, v12, v13
	v_pk_ashrrev_i16 v34, 15, v33 op_sel_hi:[0,1]
	v_bitop3_b32 v8, v33, v34, s32 bitop3:0x1e
	v_bfe_u32 v34, v8, 8, 8
	v_lshrrev_b32_e32 v33, 24, v8
	v_lshl_add_u32 v34, v34, 2, v222
	v_lshl_add_u32 v33, v33, 2, v222
	ds_add_u32 v34, v224 offset:36864
	ds_add_u32 v33, v224 offset:36864
	v_cvt_pk_f16_f32 v35, v4, v5
	v_pk_ashrrev_i16 v36, 15, v35 op_sel_hi:[0,1]
	v_bitop3_b32 v10, v35, v36, s32 bitop3:0x1e
	v_bfe_u32 v36, v10, 8, 8
	v_lshrrev_b32_e32 v35, 24, v10
	v_lshl_add_u32 v36, v36, 2, v222
	v_lshl_add_u32 v35, v35, 2, v222
	ds_add_u32 v36, v224 offset:36864
	ds_add_u32 v35, v224 offset:36864
	v_cvt_pk_f16_f32 v37, v14, v15
	v_pk_ashrrev_i16 v39, 15, v37 op_sel_hi:[0,1]
	v_bitop3_b32 v5, v37, v39, s32 bitop3:0x1e
	v_bfe_u32 v39, v5, 8, 8
	v_lshrrev_b32_e32 v37, 24, v5
	v_lshl_add_u32 v39, v39, 2, v222
	v_lshl_add_u32 v37, v37, 2, v222
	ds_add_u32 v39, v224 offset:36864
	ds_add_u32 v37, v224 offset:36864
	v_cvt_pk_f16_f32 v23, v20, v21
	v_cvt_pk_f16_f32 v25, v17, v19
	v_pk_ashrrev_i16 v24, 15, v23 op_sel_hi:[0,1]
	v_pk_ashrrev_i16 v27, 15, v25 op_sel_hi:[0,1]
	v_bitop3_b32 v4, v23, v24, s32 bitop3:0x1e
	v_bitop3_b32 v11, v25, v27, s32 bitop3:0x1e
	v_bfe_u32 v23, v4, 8, 8
	v_lshrrev_b32_e32 v24, 24, v4
	v_bfe_u32 v25, v11, 8, 8
	v_lshrrev_b32_e32 v27, 24, v11
	v_lshl_add_u32 v23, v23, 2, v222
	v_lshl_add_u32 v24, v24, 2, v222
	v_lshl_add_u32 v25, v25, 2, v222
	v_lshl_add_u32 v27, v27, 2, v222
	ds_add_u32 v23, v224 offset:36864
	ds_add_u32 v24, v224 offset:36864
	ds_add_u32 v25, v224 offset:36864
	ds_add_u32 v27, v224 offset:36864
	s_branch .Lidx_join
.LBB0_384:
	v_cvt_f16_f32_e32 v16, v20
	v_cvt_f16_f32_e32 v29, v21
	v_cvt_f16_f32_e32 v18, v17
	v_cvt_f16_f32_e32 v17, v19
	v_bitop3_b32 v42, v16, s7, v16 bitop3:0xc
	v_or_b32_e32 v41, 0x8000, v16
	v_cmp_gt_i16_e32 vcc, 0, v16
	v_bitop3_b32 v30, v29, s7, v29 bitop3:0xc
	v_or_b32_e32 v31, 0x8000, v29
	v_cndmask_b32_e32 v26, v41, v42, vcc
	v_cmp_gt_i16_e64 s[60:61], 0, v29
	v_bitop3_b32 v21, v18, s7, v18 bitop3:0xc
	v_or_b32_e32 v22, 0x8000, v18
	v_cmp_gt_i16_e64 s[58:59], 0, v18
	v_bitop3_b32 v19, v17, s7, v17 bitop3:0xc
	v_or_b32_e32 v20, 0x8000, v17
	v_lshrrev_b32_e32 v16, 8, v26
	v_cndmask_b32_e64 v16, v16, v233, s[24:25]
	v_cmp_gt_i16_e32 vcc, 0, v29
	v_lshl_add_u32 v16, v16, 2, v222
	v_cvt_f16_f32_e32 v14, v14
	v_cndmask_b32_e32 v23, v31, v30, vcc
	ds_add_u32 v16, v224 offset:36864
	v_cndmask_b32_e64 v16, 0, v23, s[26:27]
	v_lshrrev_b32_e32 v23, 8, v23
	v_cndmask_b32_e64 v23, v233, v23, s[26:27]
	v_lshl_add_u32 v23, v23, 2, v222
	ds_add_u32 v23, v224 offset:36864
	v_bitop3_b32 v23, v14, s7, v14 bitop3:0xc
	v_or_b32_e32 v24, 0x8000, v14
	v_cmp_gt_i16_e32 vcc, 0, v14
	v_cvt_f16_f32_e32 v15, v15
	v_cvt_f16_f32_e32 v12, v12
	v_cndmask_b32_e32 v14, v24, v23, vcc
	v_cndmask_b32_e64 v23, v14, 0, s[28:29]
	v_lshrrev_b32_e32 v14, 8, v14
	v_cndmask_b32_e64 v14, v14, v233, s[28:29]
	v_lshl_add_u32 v14, v14, 2, v222
	ds_add_u32 v14, v224 offset:36864
	v_bitop3_b32 v14, v15, s7, v15 bitop3:0xc
	v_or_b32_e32 v24, 0x8000, v15
	v_cmp_gt_i16_e32 vcc, 0, v15
	v_or_b32_e32 v15, 0x8000, v12
	v_cvt_f16_f32_e32 v13, v13
	v_cndmask_b32_e32 v14, v24, v14, vcc
	v_cndmask_b32_e64 v24, v14, 0, s[30:31]
	v_lshrrev_b32_e32 v14, 8, v14
	v_cndmask_b32_e64 v14, v14, v233, s[30:31]
	v_lshl_add_u32 v14, v14, 2, v222
	ds_add_u32 v14, v224 offset:36864
	v_bitop3_b32 v14, v12, s7, v12 bitop3:0xc
	v_cmp_gt_i16_e32 vcc, 0, v12
	v_cvt_f16_f32_e32 v10, v10
	v_cvt_f16_f32_e32 v11, v11
	v_cndmask_b32_e32 v12, v15, v14, vcc
	v_cndmask_b32_e64 v25, v12, 0, s[34:35]
	v_lshrrev_b32_e32 v12, 8, v12
	v_cndmask_b32_e64 v12, v12, v233, s[34:35]
	v_lshl_add_u32 v12, v12, 2, v222
	ds_add_u32 v12, v224 offset:36864
	v_bitop3_b32 v12, v13, s7, v13 bitop3:0xc
	v_or_b32_e32 v14, 0x8000, v13
	v_cmp_gt_i16_e32 vcc, 0, v13
	v_or_b32_e32 v13, 0x8000, v10
	v_cvt_f16_f32_e32 v8, v8
	v_cndmask_b32_e32 v12, v14, v12, vcc
	v_cndmask_b32_e64 v27, v12, 0, s[36:37]
	v_lshrrev_b32_e32 v12, 8, v12
	v_cndmask_b32_e64 v12, v12, v233, s[36:37]
	v_lshl_add_u32 v12, v12, 2, v222
	ds_add_u32 v12, v224 offset:36864
	v_bitop3_b32 v12, v10, s7, v10 bitop3:0xc
	v_cmp_gt_i16_e32 vcc, 0, v10
	v_cvt_f16_f32_e32 v9, v9
	v_cvt_f16_f32_e32 v6, v6
	v_cndmask_b32_e32 v10, v13, v12, vcc
	v_cndmask_b32_e64 v28, v10, 0, s[38:39]
	v_lshrrev_b32_e32 v10, 8, v10
	v_cndmask_b32_e64 v10, v10, v233, s[38:39]
	v_lshl_add_u32 v10, v10, 2, v222
	ds_add_u32 v10, v224 offset:36864
	v_bitop3_b32 v10, v11, s7, v11 bitop3:0xc
	v_or_b32_e32 v12, 0x8000, v11
	v_cmp_gt_i16_e32 vcc, 0, v11
	v_or_b32_e32 v11, 0x8000, v8
	v_cvt_f16_f32_e32 v7, v7
	v_cndmask_b32_e32 v10, v12, v10, vcc
	v_cndmask_b32_e64 v32, v10, 0, s[40:41]
	v_lshrrev_b32_e32 v10, 8, v10
	v_cndmask_b32_e64 v10, v10, v233, s[40:41]
	v_lshl_add_u32 v10, v10, 2, v222
	ds_add_u32 v10, v224 offset:36864
	v_bitop3_b32 v10, v8, s7, v8 bitop3:0xc
	v_cmp_gt_i16_e32 vcc, 0, v8
	v_cvt_f16_f32_e32 v4, v4
	v_cvt_f16_f32_e32 v5, v5
	v_cndmask_b32_e32 v8, v11, v10, vcc
	v_cndmask_b32_e64 v33, v8, 0, s[42:43]
	v_lshrrev_b32_e32 v8, 8, v8
	v_cndmask_b32_e64 v8, v8, v233, s[42:43]
	v_lshl_add_u32 v8, v8, 2, v222
	ds_add_u32 v8, v224 offset:36864
	v_bitop3_b32 v8, v9, s7, v9 bitop3:0xc
	v_or_b32_e32 v10, 0x8000, v9
	v_cmp_gt_i16_e32 vcc, 0, v9
	v_or_b32_e32 v9, 0x8000, v6
	v_cndmask_b32_e64 v42, v26, 0, s[24:25]
	v_cndmask_b32_e32 v8, v10, v8, vcc
	v_cndmask_b32_e64 v34, v8, 0, s[44:45]
	v_lshrrev_b32_e32 v8, 8, v8
	v_cndmask_b32_e64 v8, v8, v233, s[44:45]
	v_lshl_add_u32 v8, v8, 2, v222
	ds_add_u32 v8, v224 offset:36864
	v_bitop3_b32 v8, v6, s7, v6 bitop3:0xc
	v_cmp_gt_i16_e32 vcc, 0, v6
	v_mov_b32_e32 v26, v42
	s_nop 0
	v_cndmask_b32_e32 v6, v9, v8, vcc
	v_cndmask_b32_e64 v35, v6, 0, s[46:47]
	v_lshrrev_b32_e32 v6, 8, v6
	v_cndmask_b32_e64 v6, v6, v233, s[46:47]
	v_lshl_add_u32 v6, v6, 2, v222
	ds_add_u32 v6, v224 offset:36864
	v_bitop3_b32 v6, v7, s7, v7 bitop3:0xc
	v_or_b32_e32 v8, 0x8000, v7
	v_cmp_gt_i16_e32 vcc, 0, v7
	v_or_b32_e32 v7, 0x8000, v4
	s_nop 0
	v_cndmask_b32_e32 v6, v8, v6, vcc
	v_cndmask_b32_e64 v36, v6, 0, s[48:49]
	v_lshrrev_b32_e32 v6, 8, v6
	v_cndmask_b32_e64 v6, v6, v233, s[48:49]
	v_lshl_add_u32 v6, v6, 2, v222
	ds_add_u32 v6, v224 offset:36864
	v_bitop3_b32 v6, v4, s7, v4 bitop3:0xc
	v_cmp_gt_i16_e32 vcc, 0, v4
	s_nop 1
	v_cndmask_b32_e32 v4, v7, v6, vcc
	v_cndmask_b32_e64 v37, v4, 0, s[50:51]
	v_lshrrev_b32_e32 v4, 8, v4
	v_cndmask_b32_e64 v4, v4, v233, s[50:51]
	v_lshl_add_u32 v4, v4, 2, v222
	ds_add_u32 v4, v224 offset:36864
	v_bitop3_b32 v4, v5, s7, v5 bitop3:0xc
	v_or_b32_e32 v6, 0x8000, v5
	v_cmp_gt_i16_e32 vcc, 0, v5
	s_nop 1
	v_cndmask_b32_e32 v4, v6, v4, vcc
	v_cndmask_b32_e64 v39, v4, 0, s[52:53]
	v_lshrrev_b32_e32 v4, 8, v4
	v_cndmask_b32_e64 v4, v4, v233, s[52:53]
	v_lshl_add_u32 v4, v4, 2, v222
	v_cmp_gt_i16_e32 vcc, 0, v18
	ds_add_u32 v4, v224 offset:36864
	s_nop 0
	v_cndmask_b32_e32 v4, v22, v21, vcc
	v_cndmask_b32_e64 v38, v4, 0, s[54:55]
	v_lshrrev_b32_e32 v4, 8, v4
	v_cndmask_b32_e64 v4, v4, v233, s[54:55]
	v_lshl_add_u32 v4, v4, 2, v222
	ds_add_u32 v4, v224 offset:36864
	v_cmp_gt_i16_e32 vcc, 0, v17
	s_nop 1
	v_cndmask_b32_e32 v4, v20, v19, vcc
	v_cndmask_b32_e64 v40, v4, 0, s[56:57]
	v_lshrrev_b32_e32 v4, 8, v4
	v_cndmask_b32_e64 v41, v4, v233, s[56:57]

.Lst_382:
	s_cmp_eq_u32 s81, s0
	v_mfma_f32_32x32x16_bf16 v[10:25], v[68:71], v[84:87], 0
	v_mfma_f32_32x32x16_bf16 v[10:25], v[64:67], v[88:91], v[10:25]
	v_mfma_f32_32x32x16_bf16 v[10:25], v[60:63], v[92:95], v[10:25]
	v_mfma_f32_32x32x16_bf16 v[10:25], v[56:59], v[96:99], v[10:25]
	s_nop 11
	v_fma_f32 v48, |v10|, v2, 0
	v_fma_f32 v49, |v11|, v2, 0
	v_fma_f32 v50, |v12|, v2, 0
	v_fma_f32 v51, |v13|, v2, 0
	v_fma_f32 v212, |v14|, v2, 0
	v_fma_f32 v213, |v15|, v2, 0
	v_fma_f32 v215, |v16|, v2, 0
	v_fma_f32 v216, |v17|, v2, 0
	v_fma_f32 v217, |v18|, v2, 0
	v_fma_f32 v228, |v19|, v2, 0
	v_mfma_f32_32x32x16_bf16 v[4:19], v[68:71], v[100:103], 0
	v_fma_f32 v229, |v20|, v2, 0
	v_fma_f32 v230, |v21|, v2, 0
	v_mfma_f32_32x32x16_bf16 v[4:19], v[64:67], v[104:107], v[4:19]
	v_fma_f32 v234, |v22|, v2, 0
	v_fma_f32 v235, |v23|, v2, 0
	v_mfma_f32_32x32x16_bf16 v[4:19], v[60:63], v[108:111], v[4:19]
	v_fma_f32 v236, |v24|, v2, 0
	v_fma_f32 v237, |v25|, v2, 0
	v_mfma_f32_32x32x16_bf16 v[4:19], v[56:59], v[112:115], v[4:19]
	s_nop 11
	v_fma_f32 v48, |v4|, v249, v48
	v_mfma_f32_32x32x16_bf16 v[20:35], v[68:71], v[116:119], 0
	v_fma_f32 v49, |v5|, v249, v49
	v_fma_f32 v50, |v6|, v249, v50
	v_fma_f32 v51, |v7|, v249, v51
	v_mfma_f32_32x32x16_bf16 v[20:35], v[64:67], v[120:123], v[20:35]
	v_fma_f32 v8, |v8|, v249, v212
	v_fma_f32 v9, |v9|, v249, v213
	v_fma_f32 v10, |v10|, v249, v215
	v_fma_f32 v11, |v11|, v249, v216
	v_mfma_f32_32x32x16_bf16 v[20:35], v[60:63], v[124:127], v[20:35]
	v_fma_f32 v12, |v12|, v249, v217
	v_fma_f32 v13, |v13|, v249, v228
	v_fma_f32 v212, |v14|, v249, v229
	v_fma_f32 v213, |v15|, v249, v230
	v_fma_f32 v215, |v16|, v249, v234
	v_fma_f32 v216, |v17|, v249, v235
	v_fma_f32 v217, |v18|, v249, v236
	v_fma_f32 v228, |v19|, v249, v237
	v_mfma_f32_32x32x16_bf16 v[20:35], v[56:59], v[128:131], v[20:35]
	s_nop 11
	v_fma_f32 v24, |v24|, v250, v8
	v_fma_f32 v25, |v25|, v250, v9
	v_fma_f32 v26, |v26|, v250, v10
	v_fma_f32 v27, |v27|, v250, v11
	v_fma_f32 v28, |v28|, v250, v12
	v_fma_f32 v29, |v29|, v250, v13
	v_mfma_f32_32x32x16_bf16 v[4:19], v[68:71], v[132:135], 0
	v_fma_f32 v48, |v20|, v250, v48
	v_fma_f32 v49, |v21|, v250, v49
	v_fma_f32 v50, |v22|, v250, v50
	v_fma_f32 v51, |v23|, v250, v51
	v_mfma_f32_32x32x16_bf16 v[4:19], v[64:67], v[136:139], v[4:19]
	v_fma_f32 v212, |v30|, v250, v212
	v_mfma_f32_32x32x16_bf16 v[4:19], v[60:63], v[140:143], v[4:19]
	v_fma_f32 v213, |v31|, v250, v213
	v_fma_f32 v215, |v32|, v250, v215
	v_fma_f32 v216, |v33|, v250, v216
	v_fma_f32 v217, |v34|, v250, v217
	v_fma_f32 v228, |v35|, v250, v228
	v_mfma_f32_32x32x16_bf16 v[4:19], v[56:59], v[144:147], v[4:19]
	s_nop 11
	v_fma_f32 v229, |v8|, v251, v24
	v_fma_f32 v230, |v9|, v251, v25
	v_fma_f32 v234, |v10|, v251, v26
	v_fma_f32 v235, |v11|, v251, v27
	v_fma_f32 v236, |v12|, v251, v28
	v_fma_f32 v237, |v13|, v251, v29
	v_mfma_f32_32x32x16_bf16 v[20:35], v[68:71], v[148:151], 0
	v_fma_f32 v48, |v4|, v251, v48
	v_fma_f32 v49, |v5|, v251, v49
	v_fma_f32 v50, |v6|, v251, v50
	v_fma_f32 v51, |v7|, v251, v51
	v_mfma_f32_32x32x16_bf16 v[20:35], v[64:67], v[152:155], v[20:35]
	v_fma_f32 v212, |v14|, v251, v212
	v_mfma_f32_32x32x16_bf16 v[20:35], v[60:63], v[156:159], v[20:35]
	v_fma_f32 v213, |v15|, v251, v213
	v_fma_f32 v215, |v16|, v251, v215
	v_fma_f32 v216, |v17|, v251, v216
	v_fma_f32 v217, |v18|, v251, v217
	v_fma_f32 v228, |v19|, v251, v228
	v_mfma_f32_32x32x16_bf16 v[20:35], v[56:59], v[160:163], v[20:35]
	s_nop 11
	v_fma_f32 v20, |v20|, v252, v48
	v_fma_f32 v21, |v21|, v252, v49
	v_fma_f32 v22, |v22|, v252, v50
	v_fma_f32 v23, |v23|, v252, v51
	v_mfma_f32_32x32x16_bf16 v[36:51], v[68:71], v[164:167], 0
	v_fma_f32 v24, |v24|, v252, v229
	v_fma_f32 v25, |v25|, v252, v230
	v_mfma_f32_32x32x16_bf16 v[36:51], v[64:67], v[168:171], v[36:51]
	v_fma_f32 v26, |v26|, v252, v234
	v_fma_f32 v27, |v27|, v252, v235
	v_mfma_f32_32x32x16_bf16 v[36:51], v[60:63], v[172:175], v[36:51]
	v_fma_f32 v229, |v28|, v252, v236
	v_fma_f32 v230, |v29|, v252, v237
	v_fma_f32 v212, |v30|, v252, v212
	v_fma_f32 v213, |v31|, v252, v213
	v_fma_f32 v215, |v32|, v252, v215
	v_fma_f32 v216, |v33|, v252, v216
	v_fma_f32 v217, |v34|, v252, v217
	v_fma_f32 v228, |v35|, v252, v228
	v_mfma_f32_32x32x16_bf16 v[36:51], v[56:59], v[176:179], v[36:51]
	s_nop 11
	v_fma_f32 v234, |v36|, v253, v20
	v_fma_f32 v235, |v37|, v253, v21
	v_fma_f32 v236, |v38|, v253, v22
	v_fma_f32 v237, |v39|, v253, v23
	v_fma_f32 v40, |v40|, v253, v24
	v_fma_f32 v41, |v41|, v253, v25
	v_fma_f32 v42, |v42|, v253, v26
	v_fma_f32 v43, |v43|, v253, v27
	v_mfma_f32_32x32x16_bf16 v[12:27], v[68:71], v[180:183], 0
	v_fma_f32 v44, |v44|, v253, v229
	v_fma_f32 v45, |v45|, v253, v230
	v_mfma_f32_32x32x16_bf16 v[12:27], v[64:67], v[184:187], v[12:27]
	v_fma_f32 v46, |v46|, v253, v212
	v_fma_f32 v47, |v47|, v253, v213
	v_mfma_f32_32x32x16_bf16 v[12:27], v[60:63], v[188:191], v[12:27]
	v_fma_f32 v48, |v48|, v253, v215
	v_fma_f32 v49, |v49|, v253, v216
	v_fma_f32 v50, |v50|, v253, v217
	v_fma_f32 v51, |v51|, v253, v228
	v_mfma_f32_32x32x16_bf16 v[12:27], v[56:59], v[192:195], v[12:27]
	s_nop 11
	v_fma_f32 v212, |v12|, v223, v234
	v_fma_f32 v213, |v13|, v223, v235
	v_fma_f32 v215, |v14|, v223, v236
	v_fma_f32 v216, |v15|, v223, v237
	v_fma_f32 v217, |v16|, v223, v40
	v_fma_f32 v228, |v17|, v223, v41
	v_fma_f32 v229, |v18|, v223, v42
	v_fma_f32 v230, |v19|, v223, v43
	v_mfma_f32_32x32x16_bf16 v[4:19], v[68:71], v[196:199], 0
	v_fma_f32 v234, |v20|, v223, v44
	v_fma_f32 v235, |v21|, v223, v45
	v_mfma_f32_32x32x16_bf16 v[4:19], v[64:67], v[200:203], v[4:19]
	v_fma_f32 v236, |v22|, v223, v46
	v_fma_f32 v237, |v23|, v223, v47
	v_mfma_f32_32x32x16_bf16 v[4:19], v[60:63], v[204:207], v[4:19]
	v_fma_f32 v48, |v24|, v223, v48
	v_fma_f32 v49, |v25|, v223, v49
	v_fma_f32 v50, |v26|, v223, v50
	v_fma_f32 v51, |v27|, v223, v51
	v_mfma_f32_32x32x16_bf16 v[4:19], v[56:59], v[208:211], v[4:19]
	ds_read_b128 v[20:23], v214 offset:32768
	ds_read_b128 v[36:39], v214 offset:33792
	ds_read_b128 v[40:43], v214 offset:34816
	ds_read_b128 v[44:47], v214 offset:35840
	s_waitcnt lgkmcnt(3)
	v_mfma_f32_32x32x16_bf16 v[20:35], v[68:71], v[20:23], 0
	s_nop 5
	v_fma_f32 v212, |v4|, v219, v212
	v_fma_f32 v213, |v5|, v219, v213
	v_fma_f32 v4, |v6|, v219, v215
	v_fma_f32 v5, |v7|, v219, v216
	s_waitcnt lgkmcnt(2)
	v_mfma_f32_32x32x16_bf16 v[20:35], v[64:67], v[36:39], v[20:35]
	v_fma_f32 v6, |v8|, v219, v217
	v_fma_f32 v7, |v9|, v219, v228
	v_fma_f32 v8, |v10|, v219, v229
	v_fma_f32 v9, |v11|, v219, v230
	s_waitcnt lgkmcnt(1)
	v_mfma_f32_32x32x16_bf16 v[20:35], v[60:63], v[40:43], v[20:35]
	v_fma_f32 v36, |v12|, v219, v234
	v_fma_f32 v37, |v13|, v219, v235
	v_fma_f32 v38, |v14|, v219, v236
	v_fma_f32 v39, |v15|, v219, v237
	s_waitcnt lgkmcnt(0)
	v_mfma_f32_32x32x16_bf16 v[20:35], v[56:59], v[44:47], v[20:35]
	v_fma_f32 v16, |v16|, v219, v48
	v_fma_f32 v17, |v17|, v219, v49
	s_nop 9
	v_add_f32_e32 v20, v212, v20
	v_pk_add_f32 v[14:15], v[4:5], v[22:23]
	v_pk_add_f32 v[4:5], v[32:33], v[16:17]
	v_fma_f32 v18, |v18|, v219, v50
	v_fma_f32 v19, |v19|, v219, v51
	v_add_f32_e32 v21, v213, v21
	v_add_f32_e32 v17, v34, v18
	v_add_f32_e32 v19, v35, v19
	v_pk_add_f32 v[10:11], v[8:9], v[26:27]
	v_pk_add_f32 v[8:9], v[36:37], v[28:29]
	v_pk_add_f32 v[12:13], v[6:7], v[24:25]
	v_pk_add_f32 v[6:7], v[38:39], v[30:31]
	s_cbranch_scc1 .Lst_384
	v_cvt_pk_f16_f32 v23, v6, v7
	v_pk_ashrrev_i16 v24, 15, v23 op_sel_hi:[0,1]
	v_bitop3_b32 v7, v23, v24, s32 bitop3:0x1e
	v_bfe_u32 v24, v7, 8, 8
	v_lshrrev_b32_e32 v23, 24, v7
	v_lshl_add_u32 v24, v24, 2, v222
	v_lshl_add_u32 v23, v23, 2, v222
	ds_add_u32 v24, v224 offset:36864
	ds_add_u32 v23, v224 offset:36864
	v_cvt_pk_f16_f32 v25, v8, v9
	v_pk_ashrrev_i16 v27, 15, v25 op_sel_hi:[0,1]
	v_bitop3_b32 v6, v25, v27, s32 bitop3:0x1e
	v_bfe_u32 v27, v6, 8, 8
	v_lshrrev_b32_e32 v25, 24, v6
	v_lshl_add_u32 v27, v27, 2, v222
	v_lshl_add_u32 v25, v25, 2, v222
	ds_add_u32 v27, v224 offset:36864
	ds_add_u32 v25, v224 offset:36864
	v_cvt_pk_f16_f32 v28, v10, v11
	v_pk_ashrrev_i16 v32, 15, v28 op_sel_hi:[0,1]
	v_bitop3_b32 v9, v28, v32, s32 bitop3:0x1e
	v_bfe_u32 v32, v9, 8, 8
	v_lshrrev_b32_e32 v28, 24, v9
	v_lshl_add_u32 v32, v32, 2, v222
	v_lshl_add_u32 v28, v28, 2, v222
	ds_add_u32 v32, v224 offset:36864
	ds_add_u32 v28, v224 offset:36864
	v_cvt_pk_f16_f32 v33, v12, v13
	v_pk_ashrrev_i16 v34, 15, v33 op_sel_hi:[0,1]
	v_bitop3_b32 v8, v33, v34, s32 bitop3:0x1e
	v_bfe_u32 v34, v8, 8, 8
	v_lshrrev_b32_e32 v33, 24, v8
	v_lshl_add_u32 v34, v34, 2, v222
	v_lshl_add_u32 v33, v33, 2, v222
	ds_add_u32 v34, v224 offset:36864
	ds_add_u32 v33, v224 offset:36864
	v_cvt_pk_f16_f32 v35, v4, v5
	v_pk_ashrrev_i16 v36, 15, v35 op_sel_hi:[0,1]
	v_bitop3_b32 v10, v35, v36, s32 bitop3:0x1e
	v_bfe_u32 v36, v10, 8, 8
	v_lshrrev_b32_e32 v35, 24, v10
	v_lshl_add_u32 v36, v36, 2, v222
	v_lshl_add_u32 v35, v35, 2, v222
	ds_add_u32 v36, v224 offset:36864
	ds_add_u32 v35, v224 offset:36864
	v_cvt_pk_f16_f32 v37, v14, v15
	v_pk_ashrrev_i16 v39, 15, v37 op_sel_hi:[0,1]
	v_bitop3_b32 v5, v37, v39, s32 bitop3:0x1e
	v_bfe_u32 v39, v5, 8, 8
	v_lshrrev_b32_e32 v37, 24, v5
	v_lshl_add_u32 v39, v39, 2, v222
	v_lshl_add_u32 v37, v37, 2, v222
	ds_add_u32 v39, v224 offset:36864
	ds_add_u32 v37, v224 offset:36864
	v_cvt_pk_f16_f32 v23, v20, v21
	v_cvt_pk_f16_f32 v25, v17, v19
	v_pk_ashrrev_i16 v24, 15, v23 op_sel_hi:[0,1]
	v_pk_ashrrev_i16 v27, 15, v25 op_sel_hi:[0,1]
	v_bitop3_b32 v4, v23, v24, s32 bitop3:0x1e
	v_bitop3_b32 v11, v25, v27, s32 bitop3:0x1e
	v_bfe_u32 v23, v4, 8, 8
	v_lshrrev_b32_e32 v24, 24, v4
	v_bfe_u32 v25, v11, 8, 8
	v_lshrrev_b32_e32 v27, 24, v11
	v_lshl_add_u32 v23, v23, 2, v222
	v_lshl_add_u32 v24, v24, 2, v222
	v_lshl_add_u32 v25, v25, 2, v222
	v_lshl_add_u32 v27, v27, 2, v222
	ds_add_u32 v23, v224 offset:36864
	ds_add_u32 v24, v224 offset:36864
	ds_add_u32 v25, v224 offset:36864
	ds_add_u32 v27, v224 offset:36864
	s_branch .Lidx_join_b
